# cache policy: nt on all prep-phase output stores (dword as well as dwordx4)
# baseline (speedup 1.0000x reference)
; __device__ __forceinline__ void gla_pass_a(KP Pk, Frame& F, int l, int it, LAS unsigned char* wl) {
;     ...
;         float* sl = cg < GGRP ? (float*)(ws + WS_GSL) + ((size_t)seq * NCH + c) * 2048 : (float*)(ws + WS_GGS) + ((size_t)seq * NGRP + g) * 2048;
;         float* al = cg < GGRP ? (float*)(ws + WS_GAE) + ((size_t)seq * NCH + c) * 32 : (float*)(ws + WS_GGA) + ((size_t)seq * NGRP + g) * 32;
; #pragma unroll
;         for (int db = 0; db < 2; ++db)
; #pragma unroll
;             for (int nb = 0; nb < 4; ++nb)
; #pragma unroll
;                 for (int i = 0; i < 4; ++i) sl[(16 * db + 4 * kg + i) * 64 + 16 * nb + r16] = Sr[db][nb][i];
;         if ((F.lane & 15) == 0) {
; #pragma unroll
;             for (int j = 0; j < 8; ++j) al[kg * 8 + j] = __expf(ltot[j]); }
.LBB0_345:
	s_add_i32 s27, s54, s31
	s_cmp_lg_u32 s54, 6
	s_cselect_b64 s[34:35], -1, 0
	s_ashr_i32 s37, s27, 31
	v_readlane_b32 s40, v253, 50
	s_add_u32 s46, s40, s27
	v_readlane_b32 s27, v253, 49
	s_addc_u32 s47, s27, s37
	s_lshl_b64 s[40:41], s[46:47], 13
	s_add_u32 s27, s4, s40
	s_addc_u32 s37, s5, s41
	s_cmp_eq_u32 s54, 6
	s_cselect_b64 s[48:49], -1, 0
	s_and_b64 s[40:41], s[48:49], exec
	s_cselect_b32 s41, s7, s37
	s_cselect_b32 s40, s6, s27
	v_lshl_add_u64 v[42:43], v[102:103], 2, s[40:41]
	global_store_dword v[42:43], v38, off nt
	v_lshl_add_u64 v[42:43], v[104:105], 2, s[40:41]
	v_lshl_add_u64 v[44:45], v[114:115], 2, s[40:41]
	global_store_dword v[42:43], v39, off offset:256 nt
	global_store_dword v[42:43], v40, off offset:512 nt
	global_store_dword v[42:43], v41, off offset:768 nt
	global_store_dword v[42:43], v30, off offset:64 nt
	global_store_dword v[44:45], v31, off offset:256 nt
	global_store_dword v[44:45], v32, off offset:512 nt
	global_store_dword v[44:45], v33, off offset:768 nt
	global_store_dword v[42:43], v22, off offset:128 nt
	v_lshl_add_u64 v[44:45], v[116:117], 2, s[40:41]
	global_store_dword v[44:45], v23, off offset:256 nt
	global_store_dword v[44:45], v24, off offset:512 nt
	global_store_dword v[44:45], v25, off offset:768 nt
	global_store_dword v[42:43], v14, off offset:192 nt
	v_lshl_add_u64 v[42:43], v[118:119], 2, s[40:41]
	global_store_dword v[42:43], v15, off offset:256 nt
	global_store_dword v[42:43], v16, off offset:512 nt
	global_store_dword v[42:43], v17, off offset:768 nt
	v_lshl_add_u64 v[42:43], v[106:107], 2, s[40:41]
	global_store_dword v[42:43], v34, off nt
	v_lshl_add_u64 v[42:43], v[108:109], 2, s[40:41]
	global_store_dword v[42:43], v35, off nt
	v_lshl_add_u64 v[42:43], v[110:111], 2, s[40:41]
	global_store_dword v[42:43], v36, off nt
	v_lshl_add_u64 v[42:43], v[112:113], 2, s[40:41]
	global_store_dword v[42:43], v37, off nt
	v_lshl_add_u64 v[42:43], v[120:121], 2, s[40:41]
	v_lshl_add_u64 v[44:45], v[122:123], 2, s[40:41]
	v_lshl_add_u64 v[46:47], v[124:125], 2, s[40:41]
	v_lshl_add_u64 v[48:49], v[126:127], 2, s[40:41]
	global_store_dword v[42:43], v26, off offset:64 nt
	global_store_dword v[44:45], v27, off offset:64 nt
	global_store_dword v[46:47], v28, off offset:64 nt
	global_store_dword v[48:49], v29, off offset:64 nt
	global_store_dword v[42:43], v18, off offset:128 nt
	global_store_dword v[44:45], v19, off offset:128 nt
	global_store_dword v[46:47], v20, off offset:128 nt
	global_store_dword v[48:49], v21, off offset:128 nt
	global_store_dword v[42:43], v10, off offset:192 nt
	global_store_dword v[44:45], v11, off offset:192 nt
	global_store_dword v[46:47], v12, off offset:192 nt
	global_store_dword v[48:49], v13, off offset:192 nt
	s_and_saveexec_b64 s[40:41], s[38:39]
	s_cbranch_execz .LBB0_347
	s_lshl_b64 s[46:47], s[46:47], 7
	s_add_u32 s27, s18, s46
	s_addc_u32 s37, s19, s47
	s_and_b64 s[46:47], s[48:49], exec
	v_mul_f32_e32 v1, 0x3fb8aa3b, v2
	s_cselect_b32 s37, s51, s37
	s_cselect_b32 s27, s50, s27
	v_exp_f32_e32 v42, v1
	v_mul_f32_e32 v1, 0x3fb8aa3b, v3
	v_mov_b32_e32 v44, s27
	v_mov_b32_e32 v45, s37
	v_exp_f32_e32 v43, v1
	v_mul_f32_e32 v1, 0x3fb8aa3b, v4
	v_lshl_add_u64 v[46:47], v[100:101], 2, v[44:45]
	v_exp_f32_e32 v44, v1
	v_mul_f32_e32 v1, 0x3fb8aa3b, v5
	v_exp_f32_e32 v45, v1
	v_mul_f32_e32 v1, 0x3fb8aa3b, v6
	global_store_dwordx4 v[46:47], v[42:45], off nt
	s_nop 1
	v_exp_f32_e32 v42, v1
	v_mul_f32_e32 v1, 0x3fb8aa3b, v7
	v_exp_f32_e32 v43, v1
	v_mul_f32_e32 v1, 0x3fb8aa3b, v8
	v_exp_f32_e32 v44, v1
	v_mul_f32_e32 v1, 0x3fb8aa3b, v9
	v_exp_f32_e32 v45, v1
	global_store_dwordx4 v[46:47], v[42:45], off offset:16 nt
